# attention near path: padded bias table in LDS (61 masked below, 59 far above): one clamp per row instead of 32, look-ups by immediate offsets
# baseline (speedup 1.0000x reference)
;     ...
;         if (F.tid <= 128) LUT[1 + F.tid] = lutv;
;         if (F.tid == 129) LUT[0] = -1e30f;
;         __syncthreads();
;         const float bfar = LUT[129];
.LBB0_2219:
	s_waitcnt vmcnt(7)
	s_waitcnt vmcnt(6)
	s_waitcnt vmcnt(5)
	s_waitcnt vmcnt(4)
	s_waitcnt vmcnt(0)
	ds_write_b128 v218, v[16:19]
	ds_write_b128 v219, v[20:23]
	ds_write_b128 v220, v[24:27]
	ds_write_b128 v221, v[28:31]
	v_and_b32_e32 v16, 0xffff, v8
	v_lshrrev_b32_e32 v8, 16, v8
	s_mov_b32 s2, 0xffff0000
	v_lshl_or_b32 v16, v12, 16, v16
	v_and_or_b32 v8, v12, s2, v8
	v_add_u32_e32 v12, 0x9000, v222
	ds_write2_b32 v12, v16, v8 offset1:130
	v_and_b32_e32 v8, 0xffff, v9
	v_lshrrev_b32_e32 v9, 16, v9
	v_lshl_or_b32 v8, v13, 16, v8
	v_and_or_b32 v9, v13, s2, v9
	v_add_u32_e32 v12, 0x9400, v222
	ds_write2_b32 v12, v8, v9 offset0:4 offset1:134
	v_and_b32_e32 v8, 0xffff, v10
	v_lshrrev_b32_e32 v9, 16, v10
	v_lshl_or_b32 v8, v14, 16, v8
	v_and_or_b32 v9, v14, s2, v9
	v_add_u32_e32 v10, 0x9800, v222
	ds_write2_b32 v10, v8, v9 offset0:8 offset1:138
	v_and_b32_e32 v8, 0xffff, v11
	v_lshrrev_b32_e32 v9, 16, v11
	v_lshl_or_b32 v8, v15, 16, v8
	v_and_or_b32 v9, v15, s2, v9
	v_add_u32_e32 v10, 0x9c00, v222
	ds_write2_b32 v10, v8, v9 offset0:12 offset1:142
	v_and_b32_e32 v8, 0xffff, v0
	v_lshrrev_b32_e32 v0, 16, v0
	v_lshl_or_b32 v8, v4, 16, v8
	v_and_or_b32 v0, v4, s2, v0
	v_add_u32_e32 v4, 0x9000, v223
	ds_write2_b32 v4, v8, v0 offset1:130
	v_and_b32_e32 v0, 0xffff, v1
	v_lshrrev_b32_e32 v1, 16, v1
	v_lshl_or_b32 v0, v5, 16, v0
	v_and_or_b32 v1, v5, s2, v1
	v_add_u32_e32 v4, 0x9400, v223
	ds_write2_b32 v4, v0, v1 offset0:4 offset1:134
	v_and_b32_e32 v0, 0xffff, v2
	v_lshrrev_b32_e32 v1, 16, v2
	v_lshl_or_b32 v0, v6, 16, v0
	v_and_or_b32 v1, v6, s2, v1
	v_add_u32_e32 v2, 0x9800, v223
	ds_write2_b32 v2, v0, v1 offset0:8 offset1:138
	v_and_b32_e32 v0, 0xffff, v3
	v_lshrrev_b32_e32 v1, 16, v3
	v_lshl_or_b32 v0, v7, 16, v0
	v_and_or_b32 v1, v7, s2, v1
	v_add_u32_e32 v2, 0x9c00, v223
	ds_write2_b32 v2, v0, v1 offset0:12 offset1:142
	s_and_saveexec_b64 s[2:3], s[14:15]
	ds_write_b32 v213, v33 offset:4
	ds_write_b32 v213, v33 offset:33012
	s_or_b64 exec, exec, s[2:3]
	s_and_saveexec_b64 s[2:3], s[16:17]
	v_mov_b32_e32 v0, s33
	v_mov_b32_e32 v1, 0xf149f2ca
	ds_write_b32 v0, v1
	s_or_b64 exec, exec, s[2:3]
	s_andn2_b64 vcc, exec, s[0:1]
	s_waitcnt lgkmcnt(0)
	s_barrier
	s_cbranch_vccnz .LBB0_2241
	v_mov_b32_e32 v0, s74
	ds_read_b32 v114, v0
	s_lshl_b32 s0, s4, 1
	s_mov_b32 s1, s45
	v_lshl_add_u64 v[116:117], v[144:145], 0, s[0:1]
	s_add_u32 s0, s69, s0
	s_addc_u32 s1, s89, 0
	s_lshl_b32 s2, s81, 3
	s_add_u32 s2, s70, s2
	v_mov_b64_e32 v[94:95], v[98:99]
	v_mov_b64_e32 v[90:91], v[102:103]
	v_mov_b64_e32 v[86:87], v[106:107]
	v_mov_b64_e32 v[82:83], v[110:111]
	s_addc_u32 s3, s71, 0
	s_waitcnt lgkmcnt(0)
	v_mov_b32_e32 v115, v114
	v_lshl_add_u32 v229, v230, 2, s33
	v_mov_b32_e32 v233, 0xf149f2ca
	v_cmp_gt_u32_e32 vcc, 61, v230
	s_and_saveexec_b64 s[6:7], vcc
	ds_write_b32 v229, v233 offset:32768
	s_or_b64 exec, exec, s[6:7]
	v_cmp_gt_u32_e32 vcc, 59, v230
	s_and_saveexec_b64 s[6:7], vcc
	ds_write_b32 v229, v114 offset:33528
	s_or_b64 exec, exec, s[6:7]
	s_movk_i32 s98, 0xbb
	s_add_i32 s99, s33, 32776
	s_mov_b32 s19, s68
	v_mov_b64_e32 v[96:97], v[100:101]
	v_mov_b64_e32 v[92:93], v[104:105]
	v_mov_b64_e32 v[88:89], v[108:109]
	v_mov_b64_e32 v[84:85], v[112:113]
	v_mov_b32_e32 v228, 0x3fb8aa3b
	s_mov_b32 s23, 0xf149f2ca
	s_branch .LBB0_2226

;     ...
;                 if (__any(qrel <= 64 * ck + 191)) {
; #pragma unroll
;                     for (int k2 = 0; k2 < 2; ++k2) {
;                         float bb[16];
; #pragma unroll
;                         for (int i = 0; i < 16; ++i) { const int key = 32 * (2 * ck + k2) + (i & 3) + 8 * (i >> 2) + 4 * half; const int n = qrel - key;
;                             bb[i] = LUT[1 + (n < -1 ? -1 : (n > 128 ? 128 : n))]; }
; #pragma unroll
;                         for (int i = 0; i < 16; ++i) asm volatile("" : "+v"(bb[i]));
; #pragma unroll
;                         for (int i = 0; i < 16; ++i) { const float s = sacc[k2][i] + bb[i]; sacc[k2][i] = s; mx = fmaxf(mx, s); } }
.LBB0_2230:
	v_mov_b32_e32 v64, v250
	s_waitcnt lgkmcnt(0)
	ds_read_b128 v[32:35], v251
	ds_read_b128 v[66:69], v251 offset:32
	ds_read_b128 v[70:73], v251 offset:64
	ds_read_b128 v[74:77], v251 offset:96
	ds_read_b128 v[78:81], v251 offset:4608
	ds_read_b128 v[122:125], v251 offset:4640
	v_cmp_ge_i32_e32 vcc, s22, v64
	s_waitcnt lgkmcnt(5)
	v_mfma_f32_32x32x16_bf16 v[48:63], v[32:35], v[110:113], 0
	s_waitcnt lgkmcnt(4)
	v_mfma_f32_32x32x16_bf16 v[48:63], v[66:69], v[106:109], v[48:63]
	ds_read_b128 v[66:69], v251 offset:4672
	s_waitcnt lgkmcnt(4)
	v_mfma_f32_32x32x16_bf16 v[48:63], v[70:73], v[102:105], v[48:63]
	ds_read_b128 v[70:73], v251 offset:4704
	s_waitcnt lgkmcnt(4)
	v_mfma_f32_32x32x16_bf16 v[48:63], v[74:77], v[98:101], v[48:63]
	s_waitcnt lgkmcnt(3)
	v_mfma_f32_32x32x16_bf16 v[32:47], v[78:81], v[110:113], 0
	s_waitcnt lgkmcnt(2)
	v_mfma_f32_32x32x16_bf16 v[32:47], v[122:125], v[106:109], v[32:47]
	s_waitcnt lgkmcnt(1)
	v_mfma_f32_32x32x16_bf16 v[32:47], v[66:69], v[102:105], v[32:47]
	s_waitcnt lgkmcnt(0)
	v_mfma_f32_32x32x16_bf16 v[32:47], v[70:73], v[98:101], v[32:47]
	s_cbranch_vccz .LBB0_2237
	v_add3_u32 v64, v155, v64, s21
	v_med3_i32 v235, v64, -1, s98
	v_lshl_add_u32 v235, v235, 2, s99
	ds_read_b32 v122, v235 offset:236
	ds_read_b32 v123, v235 offset:232
	ds_read_b32 v124, v235 offset:228
	ds_read_b32 v125, v235 offset:224
	ds_read_b32 v126, v235 offset:204
	ds_read_b32 v127, v235 offset:200
	ds_read_b32 v128, v235 offset:196
	ds_read_b32 v129, v235 offset:192
	ds_read_b32 v130, v235 offset:172
	ds_read_b32 v131, v235 offset:168
	ds_read_b32 v132, v235 offset:164
	ds_read_b32 v133, v235 offset:160
	ds_read_b32 v134, v235 offset:140
	ds_read_b32 v135, v235 offset:136
	ds_read_b32 v136, v235 offset:132
	ds_read_b32 v137, v235 offset:128
	s_waitcnt lgkmcnt(14)
	s_waitcnt lgkmcnt(13)
	s_waitcnt lgkmcnt(12)
	v_pk_add_f32 v[122:123], v[48:49], v[122:123]
	s_waitcnt lgkmcnt(11)
	s_waitcnt lgkmcnt(10)
	v_max3_f32 v138, v122, s23, v123
	v_pk_add_f32 v[124:125], v[50:51], v[124:125]
	s_waitcnt lgkmcnt(9)
	s_waitcnt lgkmcnt(8)
	v_max3_f32 v138, v138, v124, v125
	v_pk_add_f32 v[126:127], v[52:53], v[126:127]
	s_waitcnt lgkmcnt(7)
	s_waitcnt lgkmcnt(6)
	v_max3_f32 v138, v138, v126, v127
	v_pk_add_f32 v[128:129], v[54:55], v[128:129]
	s_waitcnt lgkmcnt(5)
	s_waitcnt lgkmcnt(4)
	v_max3_f32 v138, v138, v128, v129
	v_pk_add_f32 v[130:131], v[56:57], v[130:131]
	s_waitcnt lgkmcnt(3)
	s_waitcnt lgkmcnt(2)
	v_max3_f32 v138, v138, v130, v131
	v_pk_add_f32 v[132:133], v[58:59], v[132:133]
	s_waitcnt lgkmcnt(1)
	s_waitcnt lgkmcnt(0)
	v_max3_f32 v138, v138, v132, v133
	v_pk_add_f32 v[134:135], v[60:61], v[134:135]
	v_max3_f32 v138, v138, v134, v135
	v_pk_add_f32 v[136:137], v[62:63], v[136:137]
	v_max3_f32 v166, v138, v136, v137
	ds_read_b32 v138, v235 offset:108
	ds_read_b32 v139, v235 offset:104
	ds_read_b32 v140, v235 offset:100
	ds_read_b32 v141, v235 offset:96
	ds_read_b32 v168, v235 offset:76
	ds_read_b32 v169, v235 offset:72
	ds_read_b32 v170, v235 offset:68
	ds_read_b32 v171, v235 offset:64
	ds_read_b32 v172, v235 offset:44
	ds_read_b32 v173, v235 offset:40
	ds_read_b32 v174, v235 offset:36
	ds_read_b32 v175, v235 offset:32
	ds_read_b32 v204, v235 offset:12
	ds_read_b32 v205, v235 offset:8
	ds_read_b32 v226, v235 offset:4
	ds_read_b32 v227, v235 offset:0
	s_waitcnt lgkmcnt(14)
	s_waitcnt lgkmcnt(13)
	s_waitcnt lgkmcnt(12)
	s_waitcnt lgkmcnt(11)
	s_waitcnt lgkmcnt(10)
	s_waitcnt lgkmcnt(9)
	v_pk_add_f32 v[164:165], v[32:33], v[138:139]
	s_waitcnt lgkmcnt(8)
	v_pk_add_f32 v[168:169], v[36:37], v[168:169]
	v_max3_f32 v64, v166, v164, v165
	v_pk_add_f32 v[166:167], v[34:35], v[140:141]
	s_waitcnt lgkmcnt(7)
	s_waitcnt lgkmcnt(6)
	v_pk_add_f32 v[170:171], v[38:39], v[170:171]
	v_max3_f32 v64, v64, v166, v167
	v_max3_f32 v64, v64, v168, v169
	s_waitcnt lgkmcnt(5)
	s_waitcnt lgkmcnt(4)
	v_max3_f32 v64, v64, v170, v171
	v_pk_add_f32 v[172:173], v[40:41], v[172:173]
	v_pk_add_f32 v[174:175], v[42:43], v[174:175]
	v_max3_f32 v64, v64, v172, v173
	s_waitcnt lgkmcnt(3)
	s_waitcnt lgkmcnt(2)
	v_max3_f32 v64, v64, v174, v175
	v_pk_add_f32 v[138:139], v[44:45], v[204:205]
	s_waitcnt lgkmcnt(1)
	s_waitcnt lgkmcnt(0)
	v_max3_f32 v64, v64, v138, v139
	v_pk_add_f32 v[140:141], v[46:47], v[226:227]
	s_nop 0
	v_max3_f32 v64, v64, v140, v141
	s_cbranch_execnz .LBB0_2233
